# P0 row passes: workgroups start in four groups a fraction of a step apart (chip-wide de-phasing of load and compute phases)
# speedup vs baseline: 1.0028x; 1.0028x over previous
; #define LAS __attribute__((address_space(3)))
; __device__ __forceinline__ void phase_p0(Frame& F, const Ptrs& P) {
;     ...
;     __syncthreads();
;     { LAS float* wl = (LAS float*)F.lds;
;       for (int k = F.tid; k < DM; k += NWAVES * 64) { const float gk = P.norm_mix[k]; const float* wp = P.ev_w_in + (size_t)k * EVEN_IN + 1536; LAS float* d = wl + 8 * k + 4 * (k >> 3);
;           *(LAS f32x4*)d = *(const f32x4*)wp * gk; *(LAS f32x4*)(d + 4) = *(const f32x4*)(wp + 4) * gk; }
;       __syncthreads();
; #pragma unroll
;       for (int j = 0; j < 16; ++j) { const int k = (j < 8 ? 0 : 512) + 8 * lane + (j & 7); const LAS float* s = wl + 8 * k + 4 * (k >> 3); wf[j][0] = *(const LAS f32x4*)s; wf[j][1] = *(const LAS f32x4*)(s + 4); } }
;     float* LF = (float*)(ws + WS_LF); const float bfl = P.ev_b_f[lane & 7];
;     for (int r0 = gw * 4; r0 < TOK; r0 += NGW * 4) {
;         f32x4 a[4][4];
; #pragma unroll
;         for (int q = 0; q < 4; ++q) { const float* s = P.x + (size_t)(r0 + q) * DM + 8 * lane; a[q][0] = *(const f32x4*)s; a[q][1] = *(const f32x4*)(s + 4); a[q][2] = *(const f32x4*)(s + 512); a[q][3] = *(const f32x4*)(s + 516); }
.LBB0_204:
	v_readlane_b32 s4, v237, 3
	s_nop 3
	s_and_b32 s4, s4, 3
.Lp0wg:
	s_cmp_eq_u32 s4, 0
	s_cbranch_scc1 .Lp0wg_done
	s_sleep 80
	s_sub_u32 s4, s4, 1
	s_branch .Lp0wg
